# v36
# speedup vs baseline: 1.1304x; 1.0077x over previous
.LBB3_141:
	s_or_b64 exec, exec, s[70:71]
	v_max_f32_e32 v170, 0xff7fffff, v170
	v_sub_f32_e32 v163, v173, v170
	v_mul_f32_e32 v163, 0x3fb8aa3b, v163
	v_exp_f32_e32 v224, v163
	v_sub_f32_e32 v164, v175, v170
	v_mul_f32_e32 v164, 0x3fb8aa3b, v164
	v_exp_f32_e32 v222, v164
	v_sub_f32_e32 v163, v174, v170
	v_mul_f32_e32 v163, 0x3fb8aa3b, v163
	v_exp_f32_e32 v223, v163
	v_sub_f32_e32 v164, v195, v170
	v_mul_f32_e32 v164, 0x3fb8aa3b, v164
	v_sub_f32_e32 v163, v176, v170
	v_mul_f32_e32 v163, 0x3fb8aa3b, v163
	v_exp_f32_e32 v221, v163
	v_exp_f32_e32 v220, v164
	v_sub_f32_e32 v161, v172, v170
	v_mul_f32_e32 v161, 0x3fb8aa3b, v161
	v_sub_f32_e32 v163, v196, v170
	v_mul_f32_e32 v163, 0x3fb8aa3b, v163
	v_sub_f32_e32 v164, v197, v170
	v_exp_f32_e32 v219, v163
	v_mul_f32_e32 v164, 0x3fb8aa3b, v164
	v_exp_f32_e32 v218, v164
	v_exp_f32_e32 v225, v161
	v_sub_f32_e32 v163, v198, v170
	v_mul_f32_e32 v163, 0x3fb8aa3b, v163
	v_sub_f32_e32 v164, v199, v170
	v_exp_f32_e32 v217, v163
	v_mul_f32_e32 v164, 0x3fb8aa3b, v164
	v_exp_f32_e32 v216, v164
	v_sub_f32_e32 v163, v200, v170
	v_mul_f32_e32 v163, 0x3fb8aa3b, v163
	v_sub_f32_e32 v164, v201, v170
	v_exp_f32_e32 v215, v163
	v_mul_f32_e32 v164, 0x3fb8aa3b, v164
	v_exp_f32_e32 v214, v164
	v_add_f32_e32 v161, 0, v225
	v_sub_f32_e32 v163, v202, v170
	v_mul_f32_e32 v163, 0x3fb8aa3b, v163
	v_sub_f32_e32 v164, v203, v170
	v_exp_f32_e32 v200, v163
	v_mul_f32_e32 v164, 0x3fb8aa3b, v164
	v_exp_f32_e32 v199, v164
	v_add_f32_e32 v161, v161, v224
	v_sub_f32_e32 v163, v204, v170
	v_mul_f32_e32 v163, 0x3fb8aa3b, v163
	v_sub_f32_e32 v164, v205, v170
	v_exp_f32_e32 v198, v163
	v_mul_f32_e32 v164, 0x3fb8aa3b, v164
	v_exp_f32_e32 v196, v164
	v_add_f32_e32 v161, v161, v223
	v_sub_f32_e32 v163, v206, v170
	v_mul_f32_e32 v163, 0x3fb8aa3b, v163
	v_sub_f32_e32 v164, v207, v170
	v_exp_f32_e32 v195, v163
	v_mul_f32_e32 v164, 0x3fb8aa3b, v164
	v_exp_f32_e32 v176, v164
	v_add_f32_e32 v161, v161, v222
	v_sub_f32_e32 v163, v208, v170
	v_add_f32_e32 v161, v161, v221
	v_mul_f32_e32 v163, 0x3fb8aa3b, v163
	v_sub_f32_e32 v164, v209, v170
	v_add_f32_e32 v161, v161, v220
	v_exp_f32_e32 v175, v163
	v_mul_f32_e32 v164, 0x3fb8aa3b, v164
	v_add_f32_e32 v161, v161, v219
	v_exp_f32_e32 v174, v164
	v_add_f32_e32 v161, v161, v218
	v_add_f32_e32 v161, v161, v217
	v_add_f32_e32 v161, v161, v216
	v_sub_f32_e32 v163, v210, v170
	v_add_f32_e32 v161, v161, v215
	v_mul_f32_e32 v163, 0x3fb8aa3b, v163
	v_sub_f32_e32 v164, v211, v170
	v_add_f32_e32 v161, v161, v214
	v_exp_f32_e32 v173, v163
	v_mul_f32_e32 v164, 0x3fb8aa3b, v164
	v_add_f32_e32 v161, v161, v200
	v_exp_f32_e32 v172, v164
	v_add_f32_e32 v161, v161, v199
	v_add_f32_e32 v161, v161, v198
	v_add_f32_e32 v161, v161, v196
	v_sub_f32_e32 v163, v212, v170
	v_add_f32_e32 v161, v161, v195
	v_mul_f32_e32 v163, 0x3fb8aa3b, v163
	v_sub_f32_e32 v164, v213, v170
	v_add_f32_e32 v161, v161, v176
	v_exp_f32_e32 v163, v163
	v_mul_f32_e32 v164, 0x3fb8aa3b, v164
	v_add_f32_e32 v161, v161, v175
	v_exp_f32_e32 v171, v164
	v_add_f32_e32 v161, v161, v174
	v_add_f32_e32 v161, v161, v173
	v_add_f32_e32 v161, v161, v172
	v_cndmask_b32_e64 v164, 0, v163, s[4:5]
	v_add_f32_e32 v163, v161, v164
	v_cndmask_b32_e64 v161, 0, v171, s[52:53]
	v_add_f32_e32 v163, v163, v161
	s_and_saveexec_b64 s[54:55], s[0:1]
	s_cbranch_execz .LBB3_145
	v_lshlrev_b32_e32 v171, 2, v193
	v_lshl_or_b32 v171, v160, 5, v171
	s_lshl_b32 s69, s78, 5
	v_subrev_u32_e32 v171, s69, v171
	v_add_u32_e32 v171, s93, v171
	s_mov_b32 s69, 24
	s_mov_b64 s[70:71], 0
